# state-update read pipelining extended to two more S1 blocks (10 total)
# baseline (speedup 1.0000x reference)
.LBB0_480:
	s_and_b64 s[38:39], s[38:39], exec
	s_cselect_b32 s29, 0xc0, 0
	s_or_b32 s29, s52, s29
	s_add_i32 s38, s29, s54
	v_mad_i64_i32 v[0:1], s[38:39], s38, v205, v[140:141]
	s_mov_b32 s43, s79
	v_lshl_add_u64 v[10:11], v[0:1], 0, s[78:79]
	v_lshl_add_u64 v[0:1], v[0:1], 0, s[42:43]
	s_add_i32 s38, s29, s53
	global_load_dword v103, v[10:11], off
	global_load_dword v173, v[0:1], off offset:3072
	v_mad_i64_i32 v[0:1], s[38:39], s38, v205, v[140:141]
	v_lshl_add_u64 v[10:11], v[0:1], 0, s[78:79]
	v_lshl_add_u64 v[0:1], v[0:1], 0, s[42:43]
	s_add_i32 s38, s29, s51
	global_load_dword v105, v[10:11], off
	global_load_dword v174, v[0:1], off offset:3072
	v_mad_i64_i32 v[0:1], s[38:39], s38, v205, v[140:141]
	v_lshl_add_u64 v[10:11], v[0:1], 0, s[78:79]
	v_lshl_add_u64 v[0:1], v[0:1], 0, s[42:43]
	s_add_i32 s38, s29, s50
	global_load_dword v110, v[10:11], off
	global_load_dword v175, v[0:1], off offset:3072
	v_mad_i64_i32 v[0:1], s[38:39], s38, v205, v[140:141]
	s_waitcnt vmcnt(37)
	v_lshlrev_b32_e32 v80, 16, v5
	v_and_b32_e32 v81, 0xffff0000, v5
	v_lshl_add_u64 v[10:11], v[0:1], 0, s[78:79]
	v_lshl_add_u64 v[0:1], v[0:1], 0, s[42:43]
	s_add_i32 s38, s29, s49
	v_pk_add_f32 v[82:83], v[80:81], 0 op_sel_hi:[1,0]
	s_waitcnt vmcnt(35)
	v_lshlrev_b32_e32 v76, 16, v4
	v_and_b32_e32 v77, 0xffff0000, v4
	global_load_dword v112, v[10:11], off
	global_load_dword v176, v[0:1], off offset:3072
	v_mad_i64_i32 v[0:1], s[38:39], s38, v205, v[140:141]
	v_pk_add_f32 v[78:79], v[82:83], v[76:77]
	s_waitcnt vmcnt(35)
	v_lshlrev_b32_e32 v72, 16, v3
	v_and_b32_e32 v73, 0xffff0000, v3
	v_lshl_add_u64 v[10:11], v[0:1], 0, s[78:79]
	v_lshl_add_u64 v[0:1], v[0:1], 0, s[42:43]
	s_add_i32 s38, s29, s48
	v_pk_add_f32 v[74:75], v[78:79], v[72:73]
	s_waitcnt vmcnt(33)
	v_lshlrev_b32_e32 v68, 16, v2
	v_and_b32_e32 v69, 0xffff0000, v2
	global_load_dword v118, v[10:11], off
	global_load_dword v177, v[0:1], off offset:3072
	v_mad_i64_i32 v[0:1], s[38:39], s38, v205, v[140:141]
	v_pk_add_f32 v[70:71], v[74:75], v[68:69]
	s_waitcnt vmcnt(33)
	v_lshlrev_b32_e32 v62, 16, v9
	v_and_b32_e32 v63, 0xffff0000, v9
	v_lshl_add_u64 v[10:11], v[0:1], 0, s[78:79]
	v_lshl_add_u64 v[0:1], v[0:1], 0, s[42:43]
	s_add_i32 s38, s29, s47
	v_pk_add_f32 v[66:67], v[70:71], v[62:63]
	s_waitcnt vmcnt(31)
	v_lshlrev_b32_e32 v58, 16, v8
	v_and_b32_e32 v59, 0xffff0000, v8
	global_load_dword v119, v[10:11], off
	global_load_dword v178, v[0:1], off offset:3072
	v_mad_i64_i32 v[0:1], s[38:39], s38, v205, v[140:141]
	v_pk_add_f32 v[60:61], v[66:67], v[58:59]
	s_waitcnt vmcnt(31)
	v_lshlrev_b32_e32 v52, 16, v7
	v_and_b32_e32 v53, 0xffff0000, v7
	v_lshl_add_u64 v[10:11], v[0:1], 0, s[78:79]
	v_lshl_add_u64 v[0:1], v[0:1], 0, s[42:43]
	s_add_i32 s29, s29, s46
	v_pk_add_f32 v[56:57], v[60:61], v[52:53]
	s_waitcnt vmcnt(29)
	v_lshlrev_b32_e32 v48, 16, v6
	v_and_b32_e32 v49, 0xffff0000, v6
	global_load_dword v120, v[10:11], off
	global_load_dword v179, v[0:1], off offset:3072
	v_mad_i64_i32 v[0:1], s[38:39], s29, v205, v[140:141]
	v_pk_add_f32 v[50:51], v[56:57], v[48:49]
	v_add_u32_e32 v182, s2, v161
	v_lshl_add_u64 v[10:11], v[0:1], 0, s[78:79]
	v_lshl_add_u64 v[0:1], v[0:1], 0, s[42:43]
	ds_write_b64 v182, v[50:51]
	global_load_dword v121, v[10:11], off
	global_load_dword v180, v[0:1], off offset:3072
	s_waitcnt lgkmcnt(0)
	s_barrier
	v_add_u32_e32 v152, s0, v64
	v_add_u32_e32 v153, s23, v64
	ds_read_b128 v[36:39], v172 offset:32768
	ds_read_b128 v[40:43], v172 offset:33792
	ds_read_b128 v[4:7], v152
	ds_read_b128 v[0:3], v153
	ds_read_b128 v[244:247], v170 offset:49152
	ds_read_b128 v[248:251], v170 offset:50176
	ds_read_b128 v[252:255], v170 offset:51200
	ds_read_b128 v[196:199], v170 offset:52224
	s_waitcnt lgkmcnt(3)
	v_mfma_f32_16x16x32_bf16 v[8:11], v[36:39], v[244:247], 0
	v_add_u32_e32 v181, s24, v161
	v_pk_mul_f32 v[80:81], v[80:81], s[94:95] op_sel_hi:[1,0]
	s_mov_b32 s29, 0x42f00000
	s_waitcnt lgkmcnt(2)
	v_mfma_f32_16x16x32_bf16 v[8:11], v[40:43], v[248:251], v[8:11]
	ds_read_b128 v[244:247], v170 offset:53248
	ds_read_b128 v[248:251], v170 offset:54272
	v_pk_mul_f32 v[76:77], v[76:77], s[94:95] op_sel_hi:[1,0]
	v_pk_mul_f32 v[72:73], v[72:73], s[94:95] op_sel_hi:[1,0]
	s_waitcnt lgkmcnt(3)
	v_mfma_f32_16x16x32_bf16 v[12:15], v[36:39], v[252:255], 0
	v_mul_f32_e64 v68, v68, s94
	v_mul_f32_e64 v69, v69, s94
	v_pk_mul_f32 v[62:63], v[62:63], s[94:95] op_sel_hi:[1,0]
	v_pk_mul_f32 v[58:59], v[58:59], s[94:95] op_sel_hi:[1,0]
	s_waitcnt lgkmcnt(2)
	v_mfma_f32_16x16x32_bf16 v[12:15], v[40:43], v[196:199], v[12:15]
	ds_read_b128 v[252:255], v170 offset:55296
	ds_read_b128 v[196:199], v170 offset:56320
	v_pk_mul_f32 v[52:53], v[52:53], s[94:95] op_sel_hi:[1,0]
	v_exp_f32_e32 v80, v80
	s_waitcnt lgkmcnt(3)
	v_mfma_f32_16x16x32_bf16 v[16:19], v[36:39], v[244:247], 0
	v_exp_f32_e32 v81, v81
	v_exp_f32_e32 v76, v76
	v_exp_f32_e32 v77, v77
	s_waitcnt lgkmcnt(2)
	v_mfma_f32_16x16x32_bf16 v[16:19], v[40:43], v[248:251], v[16:19]
	ds_read_b128 v[244:247], v170 offset:57344
	ds_read_b128 v[248:251], v170 offset:58368
	v_exp_f32_e32 v72, v72
	v_exp_f32_e32 v73, v73
	s_waitcnt lgkmcnt(3)
	v_mfma_f32_16x16x32_bf16 v[20:23], v[36:39], v[252:255], 0
	v_exp_f32_e32 v68, v68
	v_exp_f32_e32 v69, v69
	v_exp_f32_e32 v62, v62
	s_waitcnt lgkmcnt(2)
	v_mfma_f32_16x16x32_bf16 v[20:23], v[40:43], v[196:199], v[20:23]
	ds_read_b128 v[252:255], v170 offset:59392
	ds_read_b128 v[196:199], v170 offset:60416
	v_exp_f32_e32 v63, v63
	v_exp_f32_e32 v58, v58
	s_waitcnt lgkmcnt(3)
	v_mfma_f32_16x16x32_bf16 v[24:27], v[36:39], v[244:247], 0
	v_exp_f32_e32 v59, v59
	v_exp_f32_e32 v52, v52
	v_exp_f32_e32 v53, v53
	s_waitcnt lgkmcnt(2)
	v_mfma_f32_16x16x32_bf16 v[24:27], v[40:43], v[248:251], v[24:27]
	ds_read_b128 v[244:247], v170 offset:61440
	ds_read_b128 v[248:251], v170 offset:62464
	v_pk_mul_f32 v[48:49], v[48:49], s[94:95] op_sel_hi:[1,0]
	v_pk_add_f32 v[80:81], v[80:81], 1.0 op_sel_hi:[1,0] neg_lo:[1,0] neg_hi:[1,0]
	s_waitcnt lgkmcnt(3)
	v_mfma_f32_16x16x32_bf16 v[28:31], v[36:39], v[252:255], 0
	v_exp_f32_e32 v48, v48
	v_exp_f32_e32 v49, v49
	v_pk_add_f32 v[76:77], v[76:77], 1.0 op_sel_hi:[1,0] neg_lo:[1,0] neg_hi:[1,0]
	s_waitcnt lgkmcnt(2)
	v_mfma_f32_16x16x32_bf16 v[28:31], v[40:43], v[196:199], v[28:31]
	ds_read_b128 v[252:255], v170 offset:63488
	ds_read_b128 v[196:199], v170 offset:64512
	v_pk_add_f32 v[72:73], v[72:73], 1.0 op_sel_hi:[1,0] neg_lo:[1,0] neg_hi:[1,0]
	v_pk_add_f32 v[68:69], v[68:69], 1.0 op_sel_hi:[1,0] neg_lo:[1,0] neg_hi:[1,0]
	s_waitcnt lgkmcnt(3)
	v_mfma_f32_16x16x32_bf16 v[32:35], v[36:39], v[244:247], 0
	v_add_f32_e64 v62, -v62, 1.0
	v_add_f32_e64 v63, -v63, 1.0
	v_pk_add_f32 v[58:59], v[58:59], 1.0 op_sel_hi:[1,0] neg_lo:[1,0] neg_hi:[1,0]
	v_pk_add_f32 v[52:53], v[52:53], 1.0 op_sel_hi:[1,0] neg_lo:[1,0] neg_hi:[1,0]
	s_waitcnt lgkmcnt(2)
	v_mfma_f32_16x16x32_bf16 v[32:35], v[40:43], v[248:251], v[32:35]
	v_pk_add_f32 v[48:49], v[48:49], 1.0 op_sel_hi:[1,0] neg_lo:[1,0] neg_hi:[1,0]
	s_mov_b64 s[38:39], -1
	s_waitcnt lgkmcnt(1)
	v_mfma_f32_16x16x32_bf16 v[36:39], v[36:39], v[252:255], 0
	s_and_b64 vcc, exec, s[20:21]
	s_waitcnt lgkmcnt(0)
	v_mfma_f32_16x16x32_bf16 v[36:39], v[40:43], v[196:199], v[36:39]
	ds_read2st64_b64 v[40:43], v181 offset1:1
	s_waitcnt lgkmcnt(0)
	v_pk_add_f32 v[40:41], v[40:41], 0 op_sel_hi:[1,0]
	s_nop 0
	v_cndmask_b32_e64 v45, 0, v41, s[4:5]
	v_cndmask_b32_e64 v44, 0, v40, s[4:5]
	v_pk_add_f32 v[46:47], v[42:43], v[44:45]
	s_nop 0
	v_cndmask_b32_e64 v45, v45, v47, s[6:7]
	v_cndmask_b32_e64 v44, v44, v46, s[6:7]
	v_pk_add_f32 v[46:47], v[40:41], v[42:43]
	ds_read2st64_b64 v[40:43], v181 offset0:2 offset1:3
	s_waitcnt lgkmcnt(0)
	v_pk_add_f32 v[54:55], v[40:41], v[44:45]
	s_nop 0
	v_cndmask_b32_e64 v45, v45, v55, s[8:9]
	v_cndmask_b32_e64 v44, v44, v54, s[8:9]
	v_pk_add_f32 v[40:41], v[46:47], v[40:41]
	v_pk_add_f32 v[46:47], v[42:43], v[44:45]
	v_pk_add_f32 v[54:55], v[40:41], v[42:43]
	ds_read2st64_b64 v[40:43], v181 offset0:4 offset1:5
	v_cndmask_b32_e64 v45, v45, v47, s[10:11]
	v_cndmask_b32_e64 v44, v44, v46, s[10:11]
	s_waitcnt lgkmcnt(0)
	v_pk_add_f32 v[46:47], v[40:41], v[44:45]
	s_nop 0
	v_cndmask_b32_e64 v45, v45, v47, s[12:13]
	v_cndmask_b32_e64 v44, v44, v46, s[12:13]
	v_pk_add_f32 v[46:47], v[42:43], v[44:45]
	v_pk_add_f32 v[40:41], v[54:55], v[40:41]
	v_cndmask_b32_e64 v85, v45, v47, s[14:15]
	v_cndmask_b32_e64 v84, v44, v46, s[14:15]
	ds_read2st64_b64 v[44:47], v181 offset0:6 offset1:7
	v_pk_add_f32 v[40:41], v[40:41], v[42:43]
	s_waitcnt lgkmcnt(0)
	v_pk_add_f32 v[146:147], v[44:45], v[84:85]
	s_nop 0
	v_cndmask_b32_e64 v85, v85, v147, s[16:17]
	v_cndmask_b32_e64 v84, v84, v146, s[16:17]
	v_pk_add_f32 v[146:147], v[46:47], v[84:85]
	v_pk_add_f32 v[40:41], v[40:41], v[44:45]
	v_cndmask_b32_e64 v85, v85, v147, s[18:19]
	v_cndmask_b32_e64 v84, v84, v146, s[18:19]
	v_pk_add_f32 v[84:85], v[84:85], v[54:55] neg_lo:[0,1] neg_hi:[0,1]
	v_pk_add_f32 v[146:147], v[40:41], v[46:47]
	v_pk_mul_f32 v[84:85], v[84:85], s[94:95] op_sel_hi:[1,0]
	s_nop 0
	v_pk_fma_f32 v[82:83], v[82:83], s[94:95], v[84:85] op_sel_hi:[1,0,1]
	v_pk_fma_f32 v[78:79], v[78:79], s[94:95], v[84:85] op_sel_hi:[1,0,1]
	v_pk_fma_f32 v[74:75], v[74:75], s[94:95], v[84:85] op_sel_hi:[1,0,1]
	v_pk_fma_f32 v[70:71], v[70:71], s[94:95], v[84:85] op_sel_hi:[1,0,1]
	v_pk_fma_f32 v[66:67], v[66:67], s[94:95], v[84:85] op_sel_hi:[1,0,1]
	v_pk_fma_f32 v[60:61], v[60:61], s[94:95], v[84:85] op_sel_hi:[1,0,1]
	v_pk_fma_f32 v[56:57], v[56:57], s[94:95], v[84:85] op_sel_hi:[1,0,1]
	v_med3_f32 v82, -v82, s29, v207
	v_med3_f32 v83, -v83, s29, v207
	v_med3_f32 v78, -v78, s29, v207
	v_med3_f32 v79, -v79, s29, v207
	v_med3_f32 v74, -v74, s29, v207
	v_med3_f32 v75, -v75, s29, v207
	v_med3_f32 v70, -v70, s29, v207
	v_med3_f32 v71, -v71, s29, v207
	v_med3_f32 v66, -v66, s29, v207
	v_med3_f32 v67, -v67, s29, v207
	v_med3_f32 v60, -v60, s29, v207
	v_med3_f32 v61, -v61, s29, v207
	v_med3_f32 v56, -v56, s29, v207
	v_med3_f32 v57, -v57, s29, v207
	v_pk_fma_f32 v[50:51], v[50:51], s[94:95], v[84:85] op_sel_hi:[1,0,1]
	v_exp_f32_e32 v82, v82
	v_exp_f32_e32 v83, v83
	v_exp_f32_e32 v78, v78
	v_exp_f32_e32 v79, v79
	v_exp_f32_e32 v74, v74
	v_exp_f32_e32 v75, v75
	v_exp_f32_e32 v70, v70
	v_exp_f32_e32 v71, v71
	v_exp_f32_e32 v66, v66
	v_exp_f32_e32 v67, v67
	v_exp_f32_e32 v60, v60
	v_exp_f32_e32 v61, v61
	v_exp_f32_e32 v56, v56
	v_exp_f32_e32 v57, v57
	v_med3_f32 v50, -v50, s29, v207
	v_med3_f32 v51, -v51, s29, v207
	v_exp_f32_e32 v50, v50
	v_exp_f32_e32 v51, v51
	v_pk_mul_f32 v[80:81], v[80:81], v[82:83]
	v_pk_mul_f32 v[76:77], v[76:77], v[78:79]
	v_pk_mul_f32 v[72:73], v[72:73], v[74:75]
	v_pk_mul_f32 v[68:69], v[68:69], v[70:71]
	v_pk_mul_f32 v[62:63], v[62:63], v[66:67]
	v_pk_mul_f32 v[58:59], v[58:59], v[60:61]
	v_pk_mul_f32 v[52:53], v[52:53], v[56:57]
	v_cvt_pk_bf16_f32 v80, v80, v81
	v_cvt_pk_bf16_f32 v76, v76, v77
	v_cvt_pk_bf16_f32 v72, v72, v73
	v_cvt_pk_bf16_f32 v68, v68, v69
	v_cvt_pk_bf16_f32 v62, v62, v63
	v_cvt_pk_bf16_f32 v58, v58, v59
	s_nop 0
	v_cvt_pk_bf16_f32 v52, v52, v53
	v_pk_mul_f32 v[48:49], v[48:49], v[50:51]
	v_and_b32_e32 v40, 0xffff, v80
	v_and_b32_e32 v41, 0xffff, v72
	v_and_b32_e32 v42, 0xffff, v62
	v_and_b32_e32 v43, 0xffff, v52
	v_cvt_pk_bf16_f32 v48, v48, v49
	v_lshl_or_b32 v40, v76, 16, v40
	v_lshl_or_b32 v41, v68, 16, v41
	v_lshl_or_b32 v42, v58, 16, v42
	v_lshl_or_b32 v43, v48, 16, v43
	v_lshrrev_b32_e32 v44, 16, v80
	v_lshrrev_b32_e32 v45, 16, v72
	v_lshrrev_b32_e32 v46, 16, v62
	v_lshrrev_b32_e32 v47, 16, v52
	v_and_or_b32 v44, v76, s95, v44
	v_and_or_b32 v45, v68, s95, v45
	v_and_or_b32 v46, v58, s95, v46
	v_and_or_b32 v47, v48, s95, v47
	ds_write_b128 v171, v[40:43]
	ds_write_b128 v171, v[44:47] offset:64
	v_and_b32_e32 v40, 0xffff, v90
	v_and_b32_e32 v41, 0xffff, v108
	v_and_b32_e32 v42, 0xffff, v113
	v_and_b32_e32 v43, 0xffff, v115
	v_lshl_or_b32 v40, v106, 16, v40
	v_lshl_or_b32 v41, v109, 16, v41
	v_lshl_or_b32 v42, v114, 16, v42
	s_waitcnt vmcnt(32)
	v_lshl_or_b32 v43, v116, 16, v43
	v_lshrrev_b32_e32 v44, 16, v90
	v_lshrrev_b32_e32 v45, 16, v108
	v_lshrrev_b32_e32 v46, 16, v113
	v_lshrrev_b32_e32 v47, 16, v115
	v_and_or_b32 v44, v106, s95, v44
	v_and_or_b32 v45, v109, s95, v45
	v_and_or_b32 v46, v114, s95, v46
	v_and_or_b32 v47, v116, s95, v47
	ds_write_b128 v171, v[40:43] offset:16384
	ds_write_b128 v171, v[44:47] offset:16448
	s_cbranch_vccnz .LBB0_482
	s_mov_b64 s[38:39], 0

.LBB0_566:
	s_and_b64 s[36:37], s[36:37], exec
	s_cselect_b32 s35, 0xc0, 0
	s_or_b32 s38, s67, s35
	s_add_i32 s35, s38, s66
	v_mad_i64_i32 v[0:1], s[36:37], s35, v205, v[126:127]
	s_mov_b32 s35, s79
	v_lshl_add_u64 v[10:11], v[0:1], 0, s[78:79]
	v_lshl_add_u64 v[0:1], v[0:1], 0, s[34:35]
	s_add_i32 s36, s38, s65
	global_load_dword v103, v[10:11], off
	global_load_dword v171, v[0:1], off offset:3072
	v_mad_i64_i32 v[0:1], s[36:37], s36, v205, v[126:127]
	v_lshl_add_u64 v[10:11], v[0:1], 0, s[78:79]
	v_lshl_add_u64 v[0:1], v[0:1], 0, s[34:35]
	s_add_i32 s36, s38, s64
	global_load_dword v105, v[10:11], off
	global_load_dword v172, v[0:1], off offset:3072
	v_mad_i64_i32 v[0:1], s[36:37], s36, v205, v[126:127]
	v_lshl_add_u64 v[10:11], v[0:1], 0, s[78:79]
	v_lshl_add_u64 v[0:1], v[0:1], 0, s[34:35]
	s_add_i32 s36, s38, s63
	global_load_dword v109, v[10:11], off
	global_load_dword v173, v[0:1], off offset:3072
	v_mad_i64_i32 v[0:1], s[36:37], s36, v205, v[126:127]
	s_waitcnt vmcnt(37)
	v_lshlrev_b32_e32 v80, 16, v5
	v_and_b32_e32 v81, 0xffff0000, v5
	v_lshl_add_u64 v[10:11], v[0:1], 0, s[78:79]
	v_lshl_add_u64 v[0:1], v[0:1], 0, s[34:35]
	s_add_i32 s36, s38, s62
	v_pk_add_f32 v[82:83], v[80:81], 0 op_sel_hi:[1,0]
	s_waitcnt vmcnt(35)
	v_lshlrev_b32_e32 v76, 16, v4
	v_and_b32_e32 v77, 0xffff0000, v4
	global_load_dword v112, v[10:11], off
	global_load_dword v174, v[0:1], off offset:3072
	v_mad_i64_i32 v[0:1], s[36:37], s36, v205, v[126:127]
	v_pk_add_f32 v[78:79], v[82:83], v[76:77]
	s_waitcnt vmcnt(35)
	v_lshlrev_b32_e32 v72, 16, v3
	v_and_b32_e32 v73, 0xffff0000, v3
	v_lshl_add_u64 v[10:11], v[0:1], 0, s[78:79]
	v_lshl_add_u64 v[0:1], v[0:1], 0, s[34:35]
	s_add_i32 s36, s38, s61
	v_pk_add_f32 v[74:75], v[78:79], v[72:73]
	s_waitcnt vmcnt(33)
	v_lshlrev_b32_e32 v68, 16, v2
	v_and_b32_e32 v69, 0xffff0000, v2
	global_load_dword v118, v[10:11], off
	global_load_dword v175, v[0:1], off offset:3072
	v_mad_i64_i32 v[0:1], s[36:37], s36, v205, v[126:127]
	v_pk_add_f32 v[70:71], v[74:75], v[68:69]
	s_waitcnt vmcnt(33)
	v_lshlrev_b32_e32 v62, 16, v9
	v_and_b32_e32 v63, 0xffff0000, v9
	v_lshl_add_u64 v[10:11], v[0:1], 0, s[78:79]
	v_lshl_add_u64 v[0:1], v[0:1], 0, s[34:35]
	s_add_i32 s36, s38, s60
	v_pk_add_f32 v[66:67], v[70:71], v[62:63]
	s_waitcnt vmcnt(31)
	v_lshlrev_b32_e32 v58, 16, v8
	v_and_b32_e32 v59, 0xffff0000, v8
	global_load_dword v119, v[10:11], off
	global_load_dword v176, v[0:1], off offset:3072
	v_mad_i64_i32 v[0:1], s[36:37], s36, v205, v[126:127]
	v_pk_add_f32 v[60:61], v[66:67], v[58:59]
	s_waitcnt vmcnt(31)
	v_lshlrev_b32_e32 v52, 16, v7
	v_and_b32_e32 v53, 0xffff0000, v7
	v_lshl_add_u64 v[10:11], v[0:1], 0, s[78:79]
	v_lshl_add_u64 v[0:1], v[0:1], 0, s[34:35]
	s_add_i32 s38, s38, s59
	v_pk_add_f32 v[56:57], v[60:61], v[52:53]
	s_waitcnt vmcnt(29)
	v_lshlrev_b32_e32 v48, 16, v6
	v_and_b32_e32 v49, 0xffff0000, v6
	global_load_dword v120, v[10:11], off
	global_load_dword v177, v[0:1], off offset:3072
	v_mad_i64_i32 v[0:1], s[36:37], s38, v205, v[126:127]
	v_pk_add_f32 v[50:51], v[56:57], v[48:49]
	v_add_u32_e32 v180, s56, v124
	v_lshl_add_u64 v[10:11], v[0:1], 0, s[78:79]
	v_lshl_add_u64 v[0:1], v[0:1], 0, s[34:35]
	ds_write_b64 v180, v[50:51]
	global_load_dword v121, v[10:11], off
	global_load_dword v178, v[0:1], off offset:3072
	s_waitcnt lgkmcnt(0)
	s_barrier
	v_add_u32_e32 v152, s1, v125
	v_add_u32_e32 v153, s22, v125
	ds_read_b128 v[36:39], v170 offset:32768
	ds_read_b128 v[40:43], v170 offset:33792
	ds_read_b128 v[4:7], v152
	ds_read_b128 v[0:3], v153
	ds_read_b128 v[244:247], v160 offset:49152
	ds_read_b128 v[248:251], v160 offset:50176
	ds_read_b128 v[252:255], v160 offset:51200
	ds_read_b128 v[196:199], v160 offset:52224
	s_waitcnt lgkmcnt(3)
	v_mfma_f32_16x16x32_bf16 v[8:11], v[36:39], v[244:247], 0
	v_add_u32_e32 v179, s23, v124
	v_pk_mul_f32 v[80:81], v[80:81], s[94:95] op_sel_hi:[1,0]
	s_mov_b32 s34, 0x42f00000
	s_waitcnt lgkmcnt(2)
	v_mfma_f32_16x16x32_bf16 v[8:11], v[40:43], v[248:251], v[8:11]
	ds_read_b128 v[244:247], v160 offset:53248
	ds_read_b128 v[248:251], v160 offset:54272
	v_pk_mul_f32 v[76:77], v[76:77], s[94:95] op_sel_hi:[1,0]
	v_pk_mul_f32 v[72:73], v[72:73], s[94:95] op_sel_hi:[1,0]
	s_waitcnt lgkmcnt(3)
	v_mfma_f32_16x16x32_bf16 v[12:15], v[36:39], v[252:255], 0
	v_mul_f32_e64 v68, v68, s94
	v_mul_f32_e64 v69, v69, s94
	v_pk_mul_f32 v[62:63], v[62:63], s[94:95] op_sel_hi:[1,0]
	v_pk_mul_f32 v[58:59], v[58:59], s[94:95] op_sel_hi:[1,0]
	s_waitcnt lgkmcnt(2)
	v_mfma_f32_16x16x32_bf16 v[12:15], v[40:43], v[196:199], v[12:15]
	ds_read_b128 v[252:255], v160 offset:55296
	ds_read_b128 v[196:199], v160 offset:56320
	v_pk_mul_f32 v[52:53], v[52:53], s[94:95] op_sel_hi:[1,0]
	v_exp_f32_e32 v80, v80
	s_waitcnt lgkmcnt(3)
	v_mfma_f32_16x16x32_bf16 v[16:19], v[36:39], v[244:247], 0
	v_exp_f32_e32 v81, v81
	v_exp_f32_e32 v76, v76
	v_exp_f32_e32 v77, v77
	s_waitcnt lgkmcnt(2)
	v_mfma_f32_16x16x32_bf16 v[16:19], v[40:43], v[248:251], v[16:19]
	ds_read_b128 v[244:247], v160 offset:57344
	ds_read_b128 v[248:251], v160 offset:58368
	v_exp_f32_e32 v72, v72
	v_exp_f32_e32 v73, v73
	s_waitcnt lgkmcnt(3)
	v_mfma_f32_16x16x32_bf16 v[20:23], v[36:39], v[252:255], 0
	v_exp_f32_e32 v68, v68
	v_exp_f32_e32 v69, v69
	v_exp_f32_e32 v62, v62
	s_waitcnt lgkmcnt(2)
	v_mfma_f32_16x16x32_bf16 v[20:23], v[40:43], v[196:199], v[20:23]
	ds_read_b128 v[252:255], v160 offset:59392
	ds_read_b128 v[196:199], v160 offset:60416
	v_exp_f32_e32 v63, v63
	v_exp_f32_e32 v58, v58
	s_waitcnt lgkmcnt(3)
	v_mfma_f32_16x16x32_bf16 v[24:27], v[36:39], v[244:247], 0
	v_exp_f32_e32 v59, v59
	v_exp_f32_e32 v52, v52
	v_exp_f32_e32 v53, v53
	s_waitcnt lgkmcnt(2)
	v_mfma_f32_16x16x32_bf16 v[24:27], v[40:43], v[248:251], v[24:27]
	ds_read_b128 v[244:247], v160 offset:61440
	ds_read_b128 v[248:251], v160 offset:62464
	v_pk_mul_f32 v[48:49], v[48:49], s[94:95] op_sel_hi:[1,0]
	v_pk_add_f32 v[80:81], v[80:81], 1.0 op_sel_hi:[1,0] neg_lo:[1,0] neg_hi:[1,0]
	s_waitcnt lgkmcnt(3)
	v_mfma_f32_16x16x32_bf16 v[28:31], v[36:39], v[252:255], 0
	v_exp_f32_e32 v48, v48
	v_exp_f32_e32 v49, v49
	v_pk_add_f32 v[76:77], v[76:77], 1.0 op_sel_hi:[1,0] neg_lo:[1,0] neg_hi:[1,0]
	s_waitcnt lgkmcnt(2)
	v_mfma_f32_16x16x32_bf16 v[28:31], v[40:43], v[196:199], v[28:31]
	ds_read_b128 v[252:255], v160 offset:63488
	ds_read_b128 v[196:199], v160 offset:64512
	v_pk_add_f32 v[72:73], v[72:73], 1.0 op_sel_hi:[1,0] neg_lo:[1,0] neg_hi:[1,0]
	v_pk_add_f32 v[68:69], v[68:69], 1.0 op_sel_hi:[1,0] neg_lo:[1,0] neg_hi:[1,0]
	s_waitcnt lgkmcnt(3)
	v_mfma_f32_16x16x32_bf16 v[32:35], v[36:39], v[244:247], 0
	v_add_f32_e64 v62, -v62, 1.0
	v_add_f32_e64 v63, -v63, 1.0
	v_pk_add_f32 v[58:59], v[58:59], 1.0 op_sel_hi:[1,0] neg_lo:[1,0] neg_hi:[1,0]
	v_pk_add_f32 v[52:53], v[52:53], 1.0 op_sel_hi:[1,0] neg_lo:[1,0] neg_hi:[1,0]
	s_waitcnt lgkmcnt(2)
	v_mfma_f32_16x16x32_bf16 v[32:35], v[40:43], v[248:251], v[32:35]
	v_pk_add_f32 v[48:49], v[48:49], 1.0 op_sel_hi:[1,0] neg_lo:[1,0] neg_hi:[1,0]
	s_and_b64 vcc, exec, s[20:21]
	s_waitcnt lgkmcnt(1)
	v_mfma_f32_16x16x32_bf16 v[36:39], v[36:39], v[252:255], 0
	s_mov_b64 s[68:69], 0x80
	s_waitcnt lgkmcnt(0)
	v_mfma_f32_16x16x32_bf16 v[36:39], v[40:43], v[196:199], v[36:39]
	ds_read2st64_b64 v[40:43], v179 offset1:1
	s_waitcnt lgkmcnt(0)
	v_pk_add_f32 v[40:41], v[40:41], 0 op_sel_hi:[1,0]
	s_nop 0
	v_cndmask_b32_e64 v45, 0, v41, s[4:5]
	v_cndmask_b32_e64 v44, 0, v40, s[4:5]
	v_pk_add_f32 v[46:47], v[42:43], v[44:45]
	s_nop 0
	v_cndmask_b32_e64 v45, v45, v47, s[6:7]
	v_cndmask_b32_e64 v44, v44, v46, s[6:7]
	v_pk_add_f32 v[46:47], v[40:41], v[42:43]
	ds_read2st64_b64 v[40:43], v179 offset0:2 offset1:3
	s_waitcnt lgkmcnt(0)
	v_pk_add_f32 v[54:55], v[40:41], v[44:45]
	s_nop 0
	v_cndmask_b32_e64 v45, v45, v55, s[8:9]
	v_cndmask_b32_e64 v44, v44, v54, s[8:9]
	v_pk_add_f32 v[40:41], v[46:47], v[40:41]
	v_pk_add_f32 v[46:47], v[42:43], v[44:45]
	v_pk_add_f32 v[54:55], v[40:41], v[42:43]
	ds_read2st64_b64 v[40:43], v179 offset0:4 offset1:5
	v_cndmask_b32_e64 v45, v45, v47, s[10:11]
	v_cndmask_b32_e64 v44, v44, v46, s[10:11]
	s_waitcnt lgkmcnt(0)
	v_pk_add_f32 v[46:47], v[40:41], v[44:45]
	s_nop 0
	v_cndmask_b32_e64 v45, v45, v47, s[12:13]
	v_cndmask_b32_e64 v44, v44, v46, s[12:13]
	v_pk_add_f32 v[46:47], v[42:43], v[44:45]
	v_pk_add_f32 v[40:41], v[54:55], v[40:41]
	v_cndmask_b32_e64 v85, v45, v47, s[14:15]
	v_cndmask_b32_e64 v84, v44, v46, s[14:15]
	ds_read2st64_b64 v[44:47], v179 offset0:6 offset1:7
	v_pk_add_f32 v[40:41], v[40:41], v[42:43]
	s_waitcnt lgkmcnt(0)
	v_pk_add_f32 v[146:147], v[44:45], v[84:85]
	s_nop 0
	v_cndmask_b32_e64 v85, v85, v147, s[16:17]
	v_cndmask_b32_e64 v84, v84, v146, s[16:17]
	v_pk_add_f32 v[146:147], v[46:47], v[84:85]
	v_pk_add_f32 v[40:41], v[40:41], v[44:45]
	v_cndmask_b32_e64 v85, v85, v147, s[18:19]
	v_cndmask_b32_e64 v84, v84, v146, s[18:19]
	v_pk_add_f32 v[84:85], v[84:85], v[54:55] neg_lo:[0,1] neg_hi:[0,1]
	v_pk_add_f32 v[146:147], v[40:41], v[46:47]
	v_pk_mul_f32 v[84:85], v[84:85], s[94:95] op_sel_hi:[1,0]
	s_nop 0
	v_pk_fma_f32 v[82:83], v[82:83], s[94:95], v[84:85] op_sel_hi:[1,0,1]
	v_pk_fma_f32 v[78:79], v[78:79], s[94:95], v[84:85] op_sel_hi:[1,0,1]
	v_pk_fma_f32 v[74:75], v[74:75], s[94:95], v[84:85] op_sel_hi:[1,0,1]
	v_pk_fma_f32 v[70:71], v[70:71], s[94:95], v[84:85] op_sel_hi:[1,0,1]
	v_pk_fma_f32 v[66:67], v[66:67], s[94:95], v[84:85] op_sel_hi:[1,0,1]
	v_pk_fma_f32 v[60:61], v[60:61], s[94:95], v[84:85] op_sel_hi:[1,0,1]
	v_pk_fma_f32 v[56:57], v[56:57], s[94:95], v[84:85] op_sel_hi:[1,0,1]
	v_med3_f32 v82, -v82, s34, v207
	v_med3_f32 v83, -v83, s34, v207
	v_med3_f32 v78, -v78, s34, v207
	v_med3_f32 v79, -v79, s34, v207
	v_med3_f32 v74, -v74, s34, v207
	v_med3_f32 v75, -v75, s34, v207
	v_med3_f32 v70, -v70, s34, v207
	v_med3_f32 v71, -v71, s34, v207
	v_med3_f32 v66, -v66, s34, v207
	v_med3_f32 v67, -v67, s34, v207
	v_med3_f32 v60, -v60, s34, v207
	v_med3_f32 v61, -v61, s34, v207
	v_med3_f32 v56, -v56, s34, v207
	v_med3_f32 v57, -v57, s34, v207
	v_pk_fma_f32 v[50:51], v[50:51], s[94:95], v[84:85] op_sel_hi:[1,0,1]
	v_exp_f32_e32 v82, v82
	v_exp_f32_e32 v83, v83
	v_exp_f32_e32 v78, v78
	v_exp_f32_e32 v79, v79
	v_exp_f32_e32 v74, v74
	v_exp_f32_e32 v75, v75
	v_exp_f32_e32 v70, v70
	v_exp_f32_e32 v71, v71
	v_exp_f32_e32 v66, v66
	v_exp_f32_e32 v67, v67
	v_exp_f32_e32 v60, v60
	v_exp_f32_e32 v61, v61
	v_exp_f32_e32 v56, v56
	v_exp_f32_e32 v57, v57
	v_med3_f32 v50, -v50, s34, v207
	v_med3_f32 v51, -v51, s34, v207
	v_exp_f32_e32 v50, v50
	v_exp_f32_e32 v51, v51
	v_pk_mul_f32 v[80:81], v[80:81], v[82:83]
	v_pk_mul_f32 v[76:77], v[76:77], v[78:79]
	v_pk_mul_f32 v[72:73], v[72:73], v[74:75]
	v_pk_mul_f32 v[68:69], v[68:69], v[70:71]
	v_pk_mul_f32 v[62:63], v[62:63], v[66:67]
	v_pk_mul_f32 v[58:59], v[58:59], v[60:61]
	v_pk_mul_f32 v[52:53], v[52:53], v[56:57]
	v_cvt_pk_bf16_f32 v80, v80, v81
	v_cvt_pk_bf16_f32 v76, v76, v77
	v_cvt_pk_bf16_f32 v72, v72, v73
	v_cvt_pk_bf16_f32 v68, v68, v69
	v_cvt_pk_bf16_f32 v62, v62, v63
	v_cvt_pk_bf16_f32 v58, v58, v59
	s_nop 0
	v_cvt_pk_bf16_f32 v52, v52, v53
	v_pk_mul_f32 v[48:49], v[48:49], v[50:51]
	v_and_b32_e32 v40, 0xffff, v80
	v_and_b32_e32 v41, 0xffff, v72
	v_and_b32_e32 v42, 0xffff, v62
	v_and_b32_e32 v43, 0xffff, v52
	v_cvt_pk_bf16_f32 v48, v48, v49
	v_lshl_or_b32 v40, v76, 16, v40
	v_lshl_or_b32 v41, v68, 16, v41
	v_lshl_or_b32 v42, v58, 16, v42
	v_lshl_or_b32 v43, v48, 16, v43
	v_lshrrev_b32_e32 v44, 16, v80
	v_lshrrev_b32_e32 v45, 16, v72
	v_lshrrev_b32_e32 v46, 16, v62
	v_lshrrev_b32_e32 v47, 16, v52
	v_and_or_b32 v44, v76, s95, v44
	v_and_or_b32 v45, v68, s95, v45
	v_and_or_b32 v46, v58, s95, v46
	v_and_or_b32 v47, v48, s95, v47
	ds_write_b128 v161, v[40:43]
	ds_write_b128 v161, v[44:47] offset:64
	v_and_b32_e32 v40, 0xffff, v90
	v_and_b32_e32 v41, 0xffff, v108
	v_and_b32_e32 v42, 0xffff, v113
	v_and_b32_e32 v43, 0xffff, v115
	v_lshl_or_b32 v40, v107, 16, v40
	v_lshl_or_b32 v41, v110, 16, v41
	v_lshl_or_b32 v42, v114, 16, v42
	s_waitcnt vmcnt(32)
	v_lshl_or_b32 v43, v116, 16, v43
	v_lshrrev_b32_e32 v44, 16, v90
	v_lshrrev_b32_e32 v45, 16, v108
	v_lshrrev_b32_e32 v46, 16, v113
	v_lshrrev_b32_e32 v47, 16, v115
	s_mov_b64 s[34:35], -1
	v_and_or_b32 v44, v107, s95, v44
	v_and_or_b32 v45, v110, s95, v45
	v_and_or_b32 v46, v114, s95, v46
	v_and_or_b32 v47, v116, s95, v47
	ds_write_b128 v161, v[40:43] offset:16384
	ds_write_b128 v161, v[44:47] offset:16448
	s_cbranch_vccnz .LBB0_568
	s_mov_b64 s[34:35], 0
